# speedup vs baseline: 1.0066x; 1.0007x over previous
.LBB3_9:
	s_or_b64 exec, exec, s[16:17]
	s_add_i32 s16, s46, 2
	s_add_i32 s17, s46, 3
	s_cmp_eq_u32 s45, 0x3c04000
	s_cselect_b32 s47, s12, s41
	s_cselect_b32 s48, 0, s16
	s_cselect_b32 s49, s35, s42
	s_cselect_b32 s17, 1, s17
	s_add_i32 s50, s44, s45
	s_mov_b32 m0, s36
	s_nop 0
	buffer_load_dwordx4 v1, s[4:7], s50 offen lds
	s_mov_b32 m0, s37
	s_nop 0
	buffer_load_dwordx4 v204, s[4:7], s50 offen lds
	s_waitcnt lgkmcnt(0)
	s_waitcnt vmcnt(8)
	s_barrier
	s_setprio 1
	s_waitcnt lgkmcnt(0)
	v_mfma_f32_16x16x32_bf16 v[114:117], v[186:189], v[146:149], v[114:117]
	v_mfma_f32_16x16x32_bf16 v[110:113], v[186:189], v[154:157], v[110:113]
	v_mfma_f32_16x16x32_bf16 v[78:81], v[174:177], v[146:149], v[78:81]
	v_mfma_f32_16x16x32_bf16 v[74:77], v[174:177], v[154:157], v[74:77]
	v_mfma_f32_16x16x32_bf16 v[106:109], v[170:173], v[146:149], v[106:109]
	v_mfma_f32_16x16x32_bf16 v[102:105], v[170:173], v[154:157], v[102:105]
	v_mfma_f32_16x16x32_bf16 v[70:73], v[162:165], v[146:149], v[70:73]
	v_mfma_f32_16x16x32_bf16 v[66:69], v[162:165], v[154:157], v[66:69]
	v_mfma_f32_16x16x32_bf16 v[114:117], v[190:193], v[150:153], v[114:117]
	v_mfma_f32_16x16x32_bf16 v[110:113], v[190:193], v[158:161], v[110:113]
	v_mfma_f32_16x16x32_bf16 v[78:81], v[178:181], v[150:153], v[78:81]
	v_mfma_f32_16x16x32_bf16 v[74:77], v[178:181], v[158:161], v[74:77]
	v_mfma_f32_16x16x32_bf16 v[106:109], v[182:185], v[150:153], v[106:109]
	v_mfma_f32_16x16x32_bf16 v[102:105], v[182:185], v[158:161], v[102:105]
	v_mfma_f32_16x16x32_bf16 v[70:73], v[166:169], v[150:153], v[70:73]
	v_mfma_f32_16x16x32_bf16 v[66:69], v[166:169], v[158:161], v[66:69]
	s_setprio 0
	s_setprio 1
	v_mfma_f32_16x16x32_bf16 v[98:101], v[186:189], v[130:133], v[98:101]
	v_mfma_f32_16x16x32_bf16 v[18:21], v[186:189], v[138:141], v[18:21]
	v_mfma_f32_16x16x32_bf16 v[62:65], v[174:177], v[130:133], v[62:65]
	v_mfma_f32_16x16x32_bf16 v[2:5], v[174:177], v[138:141], v[2:5]
	v_mfma_f32_16x16x32_bf16 v[94:97], v[170:173], v[130:133], v[94:97]
	v_mfma_f32_16x16x32_bf16 v[26:29], v[170:173], v[138:141], v[26:29]
	v_mfma_f32_16x16x32_bf16 v[54:57], v[162:165], v[130:133], v[54:57]
	v_mfma_f32_16x16x32_bf16 v[10:13], v[162:165], v[138:141], v[10:13]
	v_mfma_f32_16x16x32_bf16 v[98:101], v[190:193], v[134:137], v[98:101]
	v_mfma_f32_16x16x32_bf16 v[18:21], v[190:193], v[142:145], v[18:21]
	v_mfma_f32_16x16x32_bf16 v[62:65], v[178:181], v[134:137], v[62:65]
	v_mfma_f32_16x16x32_bf16 v[2:5], v[178:181], v[142:145], v[2:5]
	v_mfma_f32_16x16x32_bf16 v[94:97], v[182:185], v[134:137], v[94:97]
	v_mfma_f32_16x16x32_bf16 v[26:29], v[182:185], v[142:145], v[26:29]
	v_mfma_f32_16x16x32_bf16 v[54:57], v[166:169], v[134:137], v[54:57]
	v_mfma_f32_16x16x32_bf16 v[10:13], v[166:169], v[142:145], v[10:13]
	s_setprio 0
	s_barrier
	s_lshl_b32 s49, s49, 6
	s_lshl_b32 s50, s48, 18
	s_or_b32 s51, s49, s50
	s_mov_b32 m0, s21
	s_lshl_b32 s51, s51, 1
	ds_read_b128 v[162:165], v226 offset:16384
	ds_read_b128 v[166:169], v226 offset:18432
	ds_read_b128 v[170:173], v227 offset:16384
	ds_read_b128 v[174:177], v227 offset:18432
	ds_read_b128 v[178:181], v226 offset:20480
	ds_read_b128 v[182:185], v226 offset:22528
	ds_read_b128 v[186:189], v227 offset:20480
	ds_read_b128 v[190:193], v227 offset:22528
	buffer_load_dwordx4 v199, s[8:11], s51 offen lds
	s_mov_b32 m0, s22
	s_lshl_b32 s48, s48, 22
	buffer_load_dwordx4 v205, s[8:11], s51 offen lds
	s_or_b32 s51, s49, 0x2000
	s_or_b32 s50, s51, s50
	s_lshl_b32 s50, s50, 1
	s_mov_b32 m0, s23
	s_lshl_b32 s47, s47, 7
	buffer_load_dwordx4 v199, s[8:11], s50 offen lds
	s_mov_b32 m0, s24
	s_add_i32 s48, s47, s48
	buffer_load_dwordx4 v205, s[8:11], s50 offen lds
	s_mov_b32 m0, s20
	s_nop 0
	buffer_load_dwordx4 v1, s[4:7], s48 offen lds
	s_mov_b32 m0, s25
	s_nop 0
	buffer_load_dwordx4 v204, s[4:7], s48 offen lds
	s_waitcnt lgkmcnt(0)
	s_waitcnt vmcnt(8)
	s_barrier
	s_setprio 1
	s_waitcnt lgkmcnt(0)
	v_mfma_f32_16x16x32_bf16 v[90:93], v[162:165], v[146:149], v[90:93]
	v_mfma_f32_16x16x32_bf16 v[86:89], v[162:165], v[154:157], v[86:89]
	v_mfma_f32_16x16x32_bf16 v[42:45], v[166:169], v[146:149], v[42:45]
	v_mfma_f32_16x16x32_bf16 v[38:41], v[166:169], v[154:157], v[38:41]
	v_mfma_f32_16x16x32_bf16 v[126:129], v[178:181], v[146:149], v[126:129]
	v_mfma_f32_16x16x32_bf16 v[122:125], v[178:181], v[154:157], v[122:125]
	v_mfma_f32_16x16x32_bf16 v[58:61], v[182:185], v[146:149], v[58:61]
	v_mfma_f32_16x16x32_bf16 v[50:53], v[182:185], v[154:157], v[50:53]
	v_mfma_f32_16x16x32_bf16 v[90:93], v[170:173], v[150:153], v[90:93]
	v_mfma_f32_16x16x32_bf16 v[86:89], v[170:173], v[158:161], v[86:89]
	v_mfma_f32_16x16x32_bf16 v[42:45], v[174:177], v[150:153], v[42:45]
	v_mfma_f32_16x16x32_bf16 v[38:41], v[174:177], v[158:161], v[38:41]
	v_mfma_f32_16x16x32_bf16 v[126:129], v[186:189], v[150:153], v[126:129]
	v_mfma_f32_16x16x32_bf16 v[122:125], v[186:189], v[158:161], v[122:125]
	v_mfma_f32_16x16x32_bf16 v[58:61], v[190:193], v[150:153], v[58:61]
	v_mfma_f32_16x16x32_bf16 v[50:53], v[190:193], v[158:161], v[50:53]
	s_setprio 0
	s_setprio 1
	v_mfma_f32_16x16x32_bf16 v[82:85], v[162:165], v[130:133], v[82:85]
	v_mfma_f32_16x16x32_bf16 v[22:25], v[162:165], v[138:141], v[22:25]
	v_mfma_f32_16x16x32_bf16 v[34:37], v[166:169], v[130:133], v[34:37]
	v_mfma_f32_16x16x32_bf16 v[6:9], v[166:169], v[138:141], v[6:9]
	v_mfma_f32_16x16x32_bf16 v[118:121], v[178:181], v[130:133], v[118:121]
	v_mfma_f32_16x16x32_bf16 v[30:33], v[178:181], v[138:141], v[30:33]
	v_mfma_f32_16x16x32_bf16 v[46:49], v[182:185], v[130:133], v[46:49]
	v_mfma_f32_16x16x32_bf16 v[14:17], v[182:185], v[138:141], v[14:17]
	v_mfma_f32_16x16x32_bf16 v[82:85], v[170:173], v[134:137], v[82:85]
	v_mfma_f32_16x16x32_bf16 v[22:25], v[170:173], v[142:145], v[22:25]
	v_mfma_f32_16x16x32_bf16 v[34:37], v[174:177], v[134:137], v[34:37]
	v_mfma_f32_16x16x32_bf16 v[6:9], v[174:177], v[142:145], v[6:9]
	v_mfma_f32_16x16x32_bf16 v[118:121], v[186:189], v[134:137], v[118:121]
	v_mfma_f32_16x16x32_bf16 v[30:33], v[186:189], v[142:145], v[30:33]
	v_mfma_f32_16x16x32_bf16 v[46:49], v[190:193], v[134:137], v[46:49]
	v_mfma_f32_16x16x32_bf16 v[14:17], v[190:193], v[142:145], v[14:17]
	s_setprio 0
	s_barrier
	v_add_u32_e32 v130, v218, v211
	v_add_u32_e32 v134, v218, v213
	v_add_u32_e32 v138, v219, v211
	v_add_u32_e32 v142, v219, v213
	v_add_u32_e32 v146, v220, v211
	v_add_u32_e32 v150, v220, v213
	v_add_u32_e32 v154, v221, v211
	v_add_u32_e32 v158, v221, v213
	s_addk_i32 s48, 0x4000
	s_mov_b32 m0, s26
	ds_read_b128 v[130:133], v130
	ds_read_b128 v[134:137], v134
	ds_read_b128 v[138:141], v138
	ds_read_b128 v[142:145], v142
	ds_read_b128 v[146:149], v146
	ds_read_b128 v[150:153], v150
	ds_read_b128 v[154:157], v154
	ds_read_b128 v[158:161], v158
	ds_read_b128 v[162:165], v226 offset:32768
	ds_read_b128 v[166:169], v226 offset:34816
	ds_read_b128 v[170:173], v227 offset:32768
	ds_read_b128 v[174:177], v227 offset:34816
	ds_read_b128 v[178:181], v226 offset:36864
	ds_read_b128 v[182:185], v226 offset:38912
	ds_read_b128 v[186:189], v227 offset:36864
	ds_read_b128 v[190:193], v227 offset:38912
	buffer_load_dwordx4 v1, s[4:7], s48 offen lds
	s_mov_b32 m0, s27
	s_nop 0
	buffer_load_dwordx4 v204, s[4:7], s48 offen lds
	s_waitcnt lgkmcnt(0)
	s_waitcnt vmcnt(8)
	s_barrier
	s_setprio 1
	s_waitcnt lgkmcnt(0)
	v_mfma_f32_16x16x32_bf16 v[114:117], v[162:165], v[130:133], v[114:117]
	v_mfma_f32_16x16x32_bf16 v[110:113], v[162:165], v[138:141], v[110:113]
	v_mfma_f32_16x16x32_bf16 v[78:81], v[166:169], v[130:133], v[78:81]
	v_mfma_f32_16x16x32_bf16 v[74:77], v[166:169], v[138:141], v[74:77]
	v_mfma_f32_16x16x32_bf16 v[106:109], v[178:181], v[130:133], v[106:109]
	v_mfma_f32_16x16x32_bf16 v[102:105], v[178:181], v[138:141], v[102:105]
	v_mfma_f32_16x16x32_bf16 v[70:73], v[182:185], v[130:133], v[70:73]
	v_mfma_f32_16x16x32_bf16 v[66:69], v[182:185], v[138:141], v[66:69]
	v_mfma_f32_16x16x32_bf16 v[114:117], v[170:173], v[134:137], v[114:117]
	v_mfma_f32_16x16x32_bf16 v[110:113], v[170:173], v[142:145], v[110:113]
	v_mfma_f32_16x16x32_bf16 v[78:81], v[174:177], v[134:137], v[78:81]
	v_mfma_f32_16x16x32_bf16 v[74:77], v[174:177], v[142:145], v[74:77]
	v_mfma_f32_16x16x32_bf16 v[106:109], v[186:189], v[134:137], v[106:109]
	v_mfma_f32_16x16x32_bf16 v[102:105], v[186:189], v[142:145], v[102:105]
	v_mfma_f32_16x16x32_bf16 v[70:73], v[190:193], v[134:137], v[70:73]
	v_mfma_f32_16x16x32_bf16 v[66:69], v[190:193], v[142:145], v[66:69]
	s_setprio 0
	s_setprio 1
	v_mfma_f32_16x16x32_bf16 v[98:101], v[162:165], v[146:149], v[98:101]
	v_mfma_f32_16x16x32_bf16 v[18:21], v[162:165], v[154:157], v[18:21]
	v_mfma_f32_16x16x32_bf16 v[62:65], v[166:169], v[146:149], v[62:65]
	v_mfma_f32_16x16x32_bf16 v[2:5], v[166:169], v[154:157], v[2:5]
	v_mfma_f32_16x16x32_bf16 v[94:97], v[178:181], v[146:149], v[94:97]
	v_mfma_f32_16x16x32_bf16 v[26:29], v[178:181], v[154:157], v[26:29]
	v_mfma_f32_16x16x32_bf16 v[54:57], v[182:185], v[146:149], v[54:57]
	v_mfma_f32_16x16x32_bf16 v[10:13], v[182:185], v[154:157], v[10:13]
	v_mfma_f32_16x16x32_bf16 v[98:101], v[170:173], v[150:153], v[98:101]
	v_mfma_f32_16x16x32_bf16 v[18:21], v[170:173], v[158:161], v[18:21]
	v_mfma_f32_16x16x32_bf16 v[62:65], v[174:177], v[150:153], v[62:65]
	v_mfma_f32_16x16x32_bf16 v[2:5], v[174:177], v[158:161], v[2:5]
	v_mfma_f32_16x16x32_bf16 v[94:97], v[186:189], v[150:153], v[94:97]
	v_mfma_f32_16x16x32_bf16 v[26:29], v[186:189], v[158:161], v[26:29]
	v_mfma_f32_16x16x32_bf16 v[54:57], v[190:193], v[150:153], v[54:57]
	v_mfma_f32_16x16x32_bf16 v[10:13], v[190:193], v[158:161], v[10:13]
	s_setprio 0
	s_barrier
	s_cmp_gt_u32 s46, 13
	s_cbranch_scc1 .Lp4_last
	s_lshl_b32 s48, s17, 18
	s_or_b32 s49, s49, s48
	s_mov_b32 m0, s28
	s_lshl_b32 s49, s49, 1
	ds_read_b128 v[162:165], v226 offset:49152
	ds_read_b128 v[166:169], v226 offset:51200
	ds_read_b128 v[170:173], v227 offset:49152
	ds_read_b128 v[174:177], v227 offset:51200
	ds_read_b128 v[178:181], v226 offset:53248
	ds_read_b128 v[182:185], v226 offset:55296
	ds_read_b128 v[186:189], v227 offset:53248
	ds_read_b128 v[190:193], v227 offset:55296
	buffer_load_dwordx4 v199, s[8:11], s49 offen lds
	s_mov_b32 m0, s29
	s_or_b32 s48, s51, s48
	buffer_load_dwordx4 v205, s[8:11], s49 offen lds
	s_lshl_b32 s48, s48, 1
	s_mov_b32 m0, s30
	s_lshl_b32 s17, s17, 22
	buffer_load_dwordx4 v199, s[8:11], s48 offen lds
	s_mov_b32 m0, s31
	s_add_i32 s17, s17, s47
	buffer_load_dwordx4 v205, s[8:11], s48 offen lds
	s_mov_b32 m0, s33
	s_nop 0
	buffer_load_dwordx4 v1, s[4:7], s17 offen lds
	s_mov_b32 m0, s34
	s_nop 0
	buffer_load_dwordx4 v204, s[4:7], s17 offen lds
	s_waitcnt lgkmcnt(0)
	s_waitcnt vmcnt(8)
	s_barrier
	s_setprio 1
	s_waitcnt lgkmcnt(0)
	v_mfma_f32_16x16x32_bf16 v[90:93], v[162:165], v[130:133], v[90:93]
	v_mfma_f32_16x16x32_bf16 v[86:89], v[162:165], v[138:141], v[86:89]
	v_mfma_f32_16x16x32_bf16 v[42:45], v[166:169], v[130:133], v[42:45]
	v_mfma_f32_16x16x32_bf16 v[38:41], v[166:169], v[138:141], v[38:41]
	v_mfma_f32_16x16x32_bf16 v[126:129], v[178:181], v[130:133], v[126:129]
	v_mfma_f32_16x16x32_bf16 v[122:125], v[178:181], v[138:141], v[122:125]
	v_mfma_f32_16x16x32_bf16 v[58:61], v[182:185], v[130:133], v[58:61]
	v_mfma_f32_16x16x32_bf16 v[50:53], v[182:185], v[138:141], v[50:53]
	v_mfma_f32_16x16x32_bf16 v[90:93], v[170:173], v[134:137], v[90:93]
	v_mfma_f32_16x16x32_bf16 v[86:89], v[170:173], v[142:145], v[86:89]
	v_mfma_f32_16x16x32_bf16 v[42:45], v[174:177], v[134:137], v[42:45]
	v_mfma_f32_16x16x32_bf16 v[38:41], v[174:177], v[142:145], v[38:41]
	v_mfma_f32_16x16x32_bf16 v[126:129], v[186:189], v[134:137], v[126:129]
	v_mfma_f32_16x16x32_bf16 v[122:125], v[186:189], v[142:145], v[122:125]
	v_mfma_f32_16x16x32_bf16 v[58:61], v[190:193], v[134:137], v[58:61]
	v_mfma_f32_16x16x32_bf16 v[50:53], v[190:193], v[142:145], v[50:53]
	s_setprio 0
	s_setprio 1
	v_mfma_f32_16x16x32_bf16 v[82:85], v[162:165], v[146:149], v[82:85]
	v_mfma_f32_16x16x32_bf16 v[22:25], v[162:165], v[154:157], v[22:25]
	v_mfma_f32_16x16x32_bf16 v[34:37], v[166:169], v[146:149], v[34:37]
	v_mfma_f32_16x16x32_bf16 v[6:9], v[166:169], v[154:157], v[6:9]
	v_mfma_f32_16x16x32_bf16 v[118:121], v[178:181], v[146:149], v[118:121]
	v_mfma_f32_16x16x32_bf16 v[30:33], v[178:181], v[154:157], v[30:33]
	v_mfma_f32_16x16x32_bf16 v[46:49], v[182:185], v[146:149], v[46:49]
	v_mfma_f32_16x16x32_bf16 v[14:17], v[182:185], v[154:157], v[14:17]
	v_mfma_f32_16x16x32_bf16 v[82:85], v[170:173], v[150:153], v[82:85]
	v_mfma_f32_16x16x32_bf16 v[22:25], v[170:173], v[158:161], v[22:25]
	v_mfma_f32_16x16x32_bf16 v[34:37], v[174:177], v[150:153], v[34:37]
	v_mfma_f32_16x16x32_bf16 v[6:9], v[174:177], v[158:161], v[6:9]
	v_mfma_f32_16x16x32_bf16 v[118:121], v[186:189], v[150:153], v[118:121]
	v_mfma_f32_16x16x32_bf16 v[30:33], v[186:189], v[158:161], v[30:33]
	v_mfma_f32_16x16x32_bf16 v[46:49], v[190:193], v[150:153], v[46:49]
	v_mfma_f32_16x16x32_bf16 v[14:17], v[190:193], v[158:161], v[14:17]
	s_setprio 0
	s_barrier
	s_add_i32 s45, s45, 0x800000
	s_mov_b32 s46, s16
	s_branch .LBB3_7
.Lp4_last:
	s_lshl_b32 s48, s17, 18
	s_or_b32 s49, s49, s48
	s_mov_b32 m0, s28
	s_lshl_b32 s49, s49, 1
	ds_read_b128 v[162:165], v226 offset:49152
	ds_read_b128 v[166:169], v226 offset:51200
	ds_read_b128 v[170:173], v227 offset:49152
	ds_read_b128 v[174:177], v227 offset:51200
	ds_read_b128 v[178:181], v226 offset:53248
	ds_read_b128 v[182:185], v226 offset:55296
	ds_read_b128 v[186:189], v227 offset:53248
	ds_read_b128 v[190:193], v227 offset:55296
	buffer_load_dwordx4 v199, s[8:11], s49 offen lds
	s_mov_b32 m0, s29
	s_or_b32 s48, s51, s48
	buffer_load_dwordx4 v205, s[8:11], s49 offen lds
	s_lshl_b32 s48, s48, 1
	s_mov_b32 m0, s30
	s_lshl_b32 s17, s17, 22
	buffer_load_dwordx4 v199, s[8:11], s48 offen lds
	s_mov_b32 m0, s31
	s_add_i32 s17, s17, s47
	buffer_load_dwordx4 v205, s[8:11], s48 offen lds
	s_mov_b32 m0, s33
	s_nop 0
	buffer_load_dwordx4 v1, s[4:7], s17 offen lds
	s_mov_b32 m0, s34
	s_nop 0
	buffer_load_dwordx4 v204, s[4:7], s17 offen lds
	s_waitcnt lgkmcnt(0)
	s_waitcnt vmcnt(8)
	s_barrier
	s_setprio 1
	s_waitcnt lgkmcnt(0)
	v_mfma_f32_16x16x32_bf16 v[90:93], v[162:165], v[130:133], v[90:93]
	v_mfma_f32_16x16x32_bf16 v[86:89], v[162:165], v[138:141], v[86:89]
	v_exp_f32_e32 v244, v114
	v_mfma_f32_16x16x32_bf16 v[42:45], v[166:169], v[130:133], v[42:45]
	v_exp_f32_e32 v245, v115
	v_mfma_f32_16x16x32_bf16 v[38:41], v[166:169], v[138:141], v[38:41]
	v_exp_f32_e32 v246, v116
	v_mfma_f32_16x16x32_bf16 v[126:129], v[178:181], v[130:133], v[126:129]
	v_exp_f32_e32 v247, v117
	v_mfma_f32_16x16x32_bf16 v[122:125], v[178:181], v[138:141], v[122:125]
	v_exp_f32_e32 v248, v78
	v_mfma_f32_16x16x32_bf16 v[58:61], v[182:185], v[130:133], v[58:61]
	v_exp_f32_e32 v249, v79
	v_mfma_f32_16x16x32_bf16 v[50:53], v[182:185], v[138:141], v[50:53]
	v_exp_f32_e32 v250, v80
	v_mfma_f32_16x16x32_bf16 v[90:93], v[170:173], v[134:137], v[90:93]
	v_exp_f32_e32 v251, v81
	v_mfma_f32_16x16x32_bf16 v[86:89], v[170:173], v[142:145], v[86:89]
	v_exp_f32_e32 v252, v106
	v_mfma_f32_16x16x32_bf16 v[42:45], v[174:177], v[134:137], v[42:45]
	v_exp_f32_e32 v253, v107
	v_mfma_f32_16x16x32_bf16 v[38:41], v[174:177], v[142:145], v[38:41]
	v_exp_f32_e32 v254, v108
	v_mfma_f32_16x16x32_bf16 v[126:129], v[186:189], v[134:137], v[126:129]
	v_exp_f32_e32 v255, v109
	v_mfma_f32_16x16x32_bf16 v[122:125], v[186:189], v[142:145], v[122:125]
	v_exp_f32_e32 v232, v70
	v_mfma_f32_16x16x32_bf16 v[58:61], v[190:193], v[134:137], v[58:61]
	v_exp_f32_e32 v233, v71
	v_mfma_f32_16x16x32_bf16 v[50:53], v[190:193], v[142:145], v[50:53]
	v_exp_f32_e32 v234, v72
	s_setprio 0
	s_setprio 1
	v_mfma_f32_16x16x32_bf16 v[82:85], v[162:165], v[146:149], v[82:85]
	v_exp_f32_e32 v235, v73
	v_mfma_f32_16x16x32_bf16 v[22:25], v[162:165], v[154:157], v[22:25]
	v_mfma_f32_16x16x32_bf16 v[34:37], v[166:169], v[146:149], v[34:37]
	v_mfma_f32_16x16x32_bf16 v[6:9], v[166:169], v[154:157], v[6:9]
	v_mfma_f32_16x16x32_bf16 v[118:121], v[178:181], v[146:149], v[118:121]
	v_mfma_f32_16x16x32_bf16 v[30:33], v[178:181], v[154:157], v[30:33]
	v_mfma_f32_16x16x32_bf16 v[46:49], v[182:185], v[146:149], v[46:49]
	v_mfma_f32_16x16x32_bf16 v[14:17], v[182:185], v[154:157], v[14:17]
	v_mfma_f32_16x16x32_bf16 v[82:85], v[170:173], v[150:153], v[82:85]
	v_mfma_f32_16x16x32_bf16 v[22:25], v[170:173], v[158:161], v[22:25]
	v_mfma_f32_16x16x32_bf16 v[34:37], v[174:177], v[150:153], v[34:37]
	v_mfma_f32_16x16x32_bf16 v[6:9], v[174:177], v[158:161], v[6:9]
	v_mfma_f32_16x16x32_bf16 v[118:121], v[186:189], v[150:153], v[118:121]
	v_mfma_f32_16x16x32_bf16 v[30:33], v[186:189], v[158:161], v[30:33]
	v_mfma_f32_16x16x32_bf16 v[46:49], v[190:193], v[150:153], v[46:49]
	v_mfma_f32_16x16x32_bf16 v[14:17], v[190:193], v[158:161], v[14:17]
	s_setprio 0
	s_barrier
.LBB3_11:
	s_lshl_b32 s58, s42, 7
	s_add_i32 s59, s41, 0x400
	s_lshr_b32 s59, s59, 6
	s_bfe_u32 s60, s20, 0x1000c
	s_add_i32 s59, s59, s60
	s_lshl_b32 s59, s59, 19
	s_add_u32 s58, s58, s59
	s_add_u32 s58, s56, s58
	s_addc_u32 s59, s57, 0
	s_add_u32 s60, s58, 0x4000
	s_addc_u32 s61, s59, 0
	s_add_u32 s62, s58, 0x100000
	s_addc_u32 s63, s59, 0
	s_add_u32 s64, s62, 0x4000
	s_addc_u32 s65, s63, 0
	s_lshr_b32 s66, s41, 7
	s_bfe_u32 s67, s20, 0x1000c
	s_add_i32 s66, s66, s67
	s_lshl_b32 s66, s66, 14
	s_lshl_b32 s67, s42, 2
	s_add_u32 s66, s66, s67
	s_add_u32 s66, s14, s66
	s_addc_u32 s67, s15, 0
	v_add_u32_e32 v172, s43, v207
	v_pk_fma_f32 v[244:245], v[244:245], -0.5, -0.5 op_sel_hi:[1,0,0]
	v_pk_fma_f32 v[246:247], v[246:247], -0.5, -0.5 op_sel_hi:[1,0,0]
	v_pk_fma_f32 v[248:249], v[248:249], -0.5, -0.5 op_sel_hi:[1,0,0]
	v_pk_fma_f32 v[250:251], v[250:251], -0.5, -0.5 op_sel_hi:[1,0,0]
	v_pk_fma_f32 v[252:253], v[252:253], -0.5, -0.5 op_sel_hi:[1,0,0]
	v_pk_fma_f32 v[254:255], v[254:255], -0.5, -0.5 op_sel_hi:[1,0,0]
	v_pk_fma_f32 v[232:233], v[232:233], -0.5, -0.5 op_sel_hi:[1,0,0]
	v_pk_fma_f32 v[234:235], v[234:235], -0.5, -0.5 op_sel_hi:[1,0,0]
	v_pk_mul_f32 v[134:135], v[244:245], v[246:247]
	v_pk_mul_f32 v[146:147], v[248:249], v[250:251]
	v_pk_mul_f32 v[180:181], v[252:253], v[254:255]
	v_pk_mul_f32 v[236:237], v[232:233], v[234:235]
	v_mul_f32_e32 v138, v134, v135
	v_mul_f32_e32 v150, v146, v147
	v_mul_f32_e32 v184, v180, v181
	v_mul_f32_e32 v240, v236, v237
	v_rcp_f32_e32 v138, v138
	v_rcp_f32_e32 v150, v150
	v_rcp_f32_e32 v184, v184
	v_rcp_f32_e32 v240, v240
	v_pk_add_f32 v[164:165], v[114:115], v[116:117]
	v_pk_add_f32 v[164:165], v[164:165], v[78:79]
	v_pk_add_f32 v[164:165], v[164:165], v[80:81]
	v_pk_add_f32 v[164:165], v[164:165], v[106:107]
	v_pk_add_f32 v[164:165], v[164:165], v[108:109]
	v_pk_add_f32 v[164:165], v[164:165], v[70:71]
	v_pk_add_f32 v[164:165], v[164:165], v[72:73]
	v_pk_mul_f32 v[162:163], v[134:135], v[146:147]
	v_pk_mul_f32 v[162:163], v[162:163], v[180:181]
	v_pk_mul_f32 v[162:163], v[162:163], v[236:237]
	v_pk_mul_f32 v[136:137], v[138:139], v[134:135] op_sel:[0,1] op_sel_hi:[0,0]
	v_pk_mul_f32 v[148:149], v[150:151], v[146:147] op_sel:[0,1] op_sel_hi:[0,0]
	v_pk_mul_f32 v[182:183], v[184:185], v[180:181] op_sel:[0,1] op_sel_hi:[0,0]
	v_pk_mul_f32 v[238:239], v[240:241], v[236:237] op_sel:[0,1] op_sel_hi:[0,0]
	v_pk_fma_f32 v[138:139], v[136:137], v[246:247], 1.0 op_sel_hi:[1,1,0]
	v_pk_fma_f32 v[140:141], v[136:137], v[244:245], 1.0 op_sel_hi:[1,1,0]
	v_pk_fma_f32 v[150:151], v[148:149], v[250:251], 1.0 op_sel_hi:[1,1,0]
	v_pk_fma_f32 v[152:153], v[148:149], v[248:249], 1.0 op_sel_hi:[1,1,0]
	v_pk_fma_f32 v[184:185], v[182:183], v[254:255], 1.0 op_sel_hi:[1,1,0]
	v_pk_fma_f32 v[186:187], v[182:183], v[252:253], 1.0 op_sel_hi:[1,1,0]
	v_pk_fma_f32 v[240:241], v[238:239], v[234:235], 1.0 op_sel_hi:[1,1,0]
	v_pk_fma_f32 v[242:243], v[238:239], v[232:233], 1.0 op_sel_hi:[1,1,0]
	v_cvt_pk_bf16_f32 v154, v138, v139
	v_cvt_pk_bf16_f32 v155, v140, v141
	v_cvt_pk_bf16_f32 v156, v150, v151
	v_cvt_pk_bf16_f32 v157, v152, v153
	v_cvt_pk_bf16_f32 v158, v184, v185
	v_cvt_pk_bf16_f32 v159, v186, v187
	v_cvt_pk_bf16_f32 v160, v240, v241
	v_cvt_pk_bf16_f32 v161, v242, v243
	ds_read_b128 v[114:117], v172
	ds_read_b128 v[78:81], v172 offset:64
	ds_read_b128 v[106:109], v172 offset:128
	ds_read_b128 v[70:73], v172 offset:192
	v_permlane16_swap_b32_e32 v154, v156
	v_permlane16_swap_b32_e32 v155, v157
	global_store_dwordx4 v228, v[154:157], s[58:59] nt
	s_bitcmp1_b32 s20, 12
	s_cbranch_scc1 .Lg1_noX
	s_barrier

	.amdhsa_kernel _Z7gemm1_kPKDF16_S0_PDF16_PKfPfS0_S1_
		.amdhsa_group_segment_fixed_size 0
		.amdhsa_private_segment_fixed_size 0
		.amdhsa_kernarg_size 56
		.amdhsa_user_sgpr_count 2
		.amdhsa_user_sgpr_dispatch_ptr 0
		.amdhsa_user_sgpr_queue_ptr 0
		.amdhsa_user_sgpr_kernarg_segment_ptr 1
		.amdhsa_user_sgpr_dispatch_id 0
		.amdhsa_user_sgpr_kernarg_preload_length 0
		.amdhsa_user_sgpr_kernarg_preload_offset 0
		.amdhsa_user_sgpr_private_segment_size 0
		.amdhsa_uses_dynamic_stack 0
		.amdhsa_enable_private_segment 0
		.amdhsa_system_sgpr_workgroup_id_x 1
		.amdhsa_system_sgpr_workgroup_id_y 0
		.amdhsa_system_sgpr_workgroup_id_z 0
		.amdhsa_system_sgpr_workgroup_info 0
		.amdhsa_system_vgpr_workitem_id 0
		.amdhsa_next_free_vgpr 256
		.amdhsa_next_free_sgpr 68
		.amdhsa_accum_offset 256
		.amdhsa_reserve_vcc 1
		.amdhsa_float_round_mode_32 0
		.amdhsa_float_round_mode_16_64 0
		.amdhsa_float_denorm_mode_32 3
		.amdhsa_float_denorm_mode_16_64 3
		.amdhsa_dx10_clamp 1
		.amdhsa_ieee_mode 1
		.amdhsa_fp16_overflow 0
		.amdhsa_tg_split 0
		.amdhsa_exception_fp_ieee_invalid_op 0
		.amdhsa_exception_fp_denorm_src 0
		.amdhsa_exception_fp_ieee_div_zero 0
		.amdhsa_exception_fp_ieee_overflow 0
		.amdhsa_exception_fp_ieee_underflow 0
		.amdhsa_exception_fp_ieee_inexact 0
		.amdhsa_exception_int_div_zero 0
	.end_amdhsa_kernel

amdhsa.kernels:
  - .agpr_count:     0
    .args:
      - .actual_access:  read_only
        .address_space:  global
        .offset:         0
        .size:           8
        .value_kind:     global_buffer
      - .actual_access:  read_only
        .address_space:  global
        .offset:         8
        .size:           8
        .value_kind:     global_buffer
      - .actual_access:  read_only
        .address_space:  global
        .offset:         16
        .size:           8
        .value_kind:     global_buffer
      - .actual_access:  write_only
        .address_space:  global
        .offset:         24
        .size:           8
        .value_kind:     global_buffer
      - .actual_access:  write_only
        .address_space:  global
        .offset:         32
        .size:           8
        .value_kind:     global_buffer
      - .actual_access:  write_only
        .address_space:  global
        .offset:         40
        .size:           8
        .value_kind:     global_buffer
      - .actual_access:  write_only
        .address_space:  global
        .offset:         48
        .size:           8
        .value_kind:     global_buffer
      - .actual_access:  read_only
        .address_space:  global
        .offset:         56
        .size:           8
        .value_kind:     global_buffer
      - .actual_access:  read_only
        .address_space:  global
        .offset:         64
        .size:           8
        .value_kind:     global_buffer
      - .actual_access:  write_only
        .address_space:  global
        .offset:         72
        .size:           8
        .value_kind:     global_buffer
    .group_segment_fixed_size: 8448
    .kernarg_segment_align: 8
    .kernarg_segment_size: 80
    .language:       OpenCL C
    .language_version:
      - 2
      - 0
    .max_flat_workgroup_size: 256
    .name:           _Z6prep_kPKfS0_S0_PDF16_S1_S1_S1_S1_S0_Pf
    .private_segment_fixed_size: 0
    .sgpr_count:     22
    .sgpr_spill_count: 0
    .symbol:         _Z6prep_kPKfS0_S0_PDF16_S1_S1_S1_S1_S0_Pf.kd
    .uniform_work_group_size: 1
    .uses_dynamic_stack: false
    .vgpr_count:     34
    .vgpr_spill_count: 0
    .wavefront_size: 64
  - .agpr_count:     0
    .args:
      - .actual_access:  read_only
        .address_space:  global
        .offset:         0
        .size:           8
        .value_kind:     global_buffer
      - .actual_access:  write_only
        .address_space:  global
        .offset:         8
        .size:           8
        .value_kind:     global_buffer
      - .actual_access:  read_only
        .address_space:  global
        .offset:         16
        .size:           8
        .value_kind:     global_buffer
      - .actual_access:  write_only
        .address_space:  global
        .offset:         24
        .size:           8
        .value_kind:     global_buffer
      - .offset:         32
        .size:           4
        .value_kind:     hidden_block_count_x
      - .offset:         36
        .size:           4
        .value_kind:     hidden_block_count_y
      - .offset:         40
        .size:           4
        .value_kind:     hidden_block_count_z
      - .offset:         44
        .size:           2
        .value_kind:     hidden_group_size_x
      - .offset:         46
        .size:           2
        .value_kind:     hidden_group_size_y
      - .offset:         48
        .size:           2
        .value_kind:     hidden_group_size_z
      - .offset:         50
        .size:           2
        .value_kind:     hidden_remainder_x
      - .offset:         52
        .size:           2
        .value_kind:     hidden_remainder_y
      - .offset:         54
        .size:           2
        .value_kind:     hidden_remainder_z
      - .offset:         72
        .size:           8
        .value_kind:     hidden_global_offset_x
      - .offset:         80
        .size:           8
        .value_kind:     hidden_global_offset_y
      - .offset:         88
        .size:           8
        .value_kind:     hidden_global_offset_z
      - .offset:         96
        .size:           2
        .value_kind:     hidden_grid_dims
    .group_segment_fixed_size: 0
    .kernarg_segment_align: 8
    .kernarg_segment_size: 288
    .language:       OpenCL C
    .language_version:
      - 2
      - 0
    .max_flat_workgroup_size: 1024
    .name:           _Z6post_kPKfPfPKDF16_PDF16_
    .private_segment_fixed_size: 0
    .sgpr_count:     14
    .sgpr_spill_count: 0
    .symbol:         _Z6post_kPKfPfPKDF16_PDF16_.kd
    .uniform_work_group_size: 1
    .uses_dynamic_stack: false
    .vgpr_count:     49
    .vgpr_spill_count: 0
    .wavefront_size: 64
  - .agpr_count:     0
    .args:
      - .actual_access:  read_only
        .address_space:  global
        .offset:         0
        .size:           8
        .value_kind:     global_buffer
      - .actual_access:  read_only
        .address_space:  global
        .offset:         8
        .size:           8
        .value_kind:     global_buffer
      - .actual_access:  write_only
        .address_space:  global
        .offset:         16
        .size:           8
        .value_kind:     global_buffer
      - .offset:         24
        .size:           4
        .value_kind:     hidden_block_count_x
      - .offset:         28
        .size:           4
        .value_kind:     hidden_block_count_y
      - .offset:         32
        .size:           4
        .value_kind:     hidden_block_count_z
      - .offset:         36
        .size:           2
        .value_kind:     hidden_group_size_x
      - .offset:         38
        .size:           2
        .value_kind:     hidden_group_size_y
      - .offset:         40
        .size:           2
        .value_kind:     hidden_group_size_z
      - .offset:         42
        .size:           2
        .value_kind:     hidden_remainder_x
      - .offset:         44
        .size:           2
        .value_kind:     hidden_remainder_y
      - .offset:         46
        .size:           2
        .value_kind:     hidden_remainder_z
      - .offset:         64
        .size:           8
        .value_kind:     hidden_global_offset_x
      - .offset:         72
        .size:           8
        .value_kind:     hidden_global_offset_y
      - .offset:         80
        .size:           8
        .value_kind:     hidden_global_offset_z
      - .offset:         88
        .size:           2
        .value_kind:     hidden_grid_dims
    .group_segment_fixed_size: 0
    .kernarg_segment_align: 8
    .kernarg_segment_size: 280
    .language:       OpenCL C
    .language_version:
      - 2
      - 0
    .max_flat_workgroup_size: 1024
    .name:           _Z8reduce_kPKDF16_PKfPf
    .private_segment_fixed_size: 0
    .sgpr_count:     22
    .sgpr_spill_count: 0
    .symbol:         _Z8reduce_kPKDF16_PKfPf.kd
    .uniform_work_group_size: 1
    .uses_dynamic_stack: false
    .vgpr_count:     42
    .vgpr_spill_count: 0
    .wavefront_size: 64
  - .agpr_count:     0
    .args:
      - .actual_access:  read_only
        .address_space:  global
        .offset:         0
        .size:           8
        .value_kind:     global_buffer
      - .actual_access:  read_only
        .address_space:  global
        .offset:         8
        .size:           8
        .value_kind:     global_buffer
      - .actual_access:  write_only
        .address_space:  global
        .offset:         16
        .size:           8
        .value_kind:     global_buffer
      - .address_space:  global
        .offset:         24
        .size:           8
        .value_kind:     global_buffer
      - .actual_access:  write_only
        .address_space:  global
        .offset:         32
        .size:           8
        .value_kind:     global_buffer
      - .actual_access:  read_only
        .address_space:  global
        .offset:         40
        .size:           8
        .value_kind:     global_buffer
      - .actual_access:  write_only
        .address_space:  global
        .offset:         48
        .size:           8
        .value_kind:     global_buffer
    .group_segment_fixed_size: 0
    .kernarg_segment_align: 8
    .kernarg_segment_size: 56
    .language:       OpenCL C
    .language_version:
      - 2
      - 0
    .max_flat_workgroup_size: 512
    .name:           _Z7gemm1_kPKDF16_S0_PDF16_PKfPfS0_S1_
    .private_segment_fixed_size: 0
    .sgpr_count:     74
    .sgpr_spill_count: 0
    .symbol:         _Z7gemm1_kPKDF16_S0_PDF16_PKfPfS0_S1_.kd
    .uniform_work_group_size: 1
    .uses_dynamic_stack: false
    .vgpr_count:     256
    .vgpr_spill_count: 0
    .wavefront_size: 64
  - .agpr_count:     0
    .args:
      - .actual_access:  read_only
        .address_space:  global
        .offset:         0
        .size:           8
        .value_kind:     global_buffer
      - .actual_access:  read_only
        .address_space:  global
        .offset:         8
        .size:           8
        .value_kind:     global_buffer
      - .offset:         16
        .size:           4
        .value_kind:     by_value
      - .offset:         20
        .size:           4
        .value_kind:     by_value
      - .offset:         24
        .size:           4
        .value_kind:     by_value
      - .offset:         28
        .size:           4
        .value_kind:     by_value
      - .actual_access:  read_only
        .address_space:  global
        .offset:         32
        .size:           8
        .value_kind:     global_buffer
      - .actual_access:  write_only
        .address_space:  global
        .offset:         40
        .size:           8
        .value_kind:     global_buffer
      - .actual_access:  read_only
        .address_space:  global
        .offset:         48
        .size:           8
        .value_kind:     global_buffer
      - .actual_access:  read_only
        .address_space:  global
        .offset:         56
        .size:           8
        .value_kind:     global_buffer
    .group_segment_fixed_size: 0
    .kernarg_segment_align: 8
    .kernarg_segment_size: 64
    .language:       OpenCL C
    .language_version:
      - 2
      - 0
    .max_flat_workgroup_size: 512
    .name:           _Z6gemm_kILi2EEvPKDF16_S1_iiiiPfPDF16_PKfS2_
    .private_segment_fixed_size: 0
    .sgpr_count:     70
    .sgpr_spill_count: 0
    .symbol:         _Z6gemm_kILi2EEvPKDF16_S1_iiiiPfPDF16_PKfS2_.kd
    .uniform_work_group_size: 1
    .uses_dynamic_stack: false
    .vgpr_count:     224
    .vgpr_spill_count: 0
    .wavefront_size: 64
  - .agpr_count:     0
    .args:
      - .actual_access:  read_only
        .address_space:  global
        .offset:         0
        .size:           8
        .value_kind:     global_buffer
      - .actual_access:  read_only
        .address_space:  global
        .offset:         8
        .size:           8
        .value_kind:     global_buffer
      - .offset:         16
        .size:           4
        .value_kind:     by_value
      - .offset:         20
        .size:           4
        .value_kind:     by_value
      - .offset:         24
        .size:           4
        .value_kind:     by_value
      - .offset:         28
        .size:           4
        .value_kind:     by_value
      - .actual_access:  read_only
        .address_space:  global
        .offset:         32
        .size:           8
        .value_kind:     global_buffer
      - .actual_access:  write_only
        .address_space:  global
        .offset:         40
        .size:           8
        .value_kind:     global_buffer
      - .actual_access:  read_only
        .address_space:  global
        .offset:         48
        .size:           8
        .value_kind:     global_buffer
      - .actual_access:  read_only
        .address_space:  global
        .offset:         56
        .size:           8
        .value_kind:     global_buffer
    .group_segment_fixed_size: 0
    .kernarg_segment_align: 8
    .kernarg_segment_size: 64
    .language:       OpenCL C
    .language_version:
      - 2
      - 0
    .max_flat_workgroup_size: 512
    .name:           _Z6gemm_kILi3EEvPKDF16_S1_iiiiPfPDF16_PKfS2_
    .private_segment_fixed_size: 0
    .sgpr_count:     51
    .sgpr_spill_count: 0
    .symbol:         _Z6gemm_kILi3EEvPKDF16_S1_iiiiPfPDF16_PKfS2_.kd
    .uniform_work_group_size: 1
    .uses_dynamic_stack: false
    .vgpr_count:     220
    .vgpr_spill_count: 0
    .wavefront_size: 64
